# DSA select collect stage regenerated: 4 VALU per key (no dump row, SGPR index constants, clamp per 8 keys), lane bits fixed at read-back
# baseline (speedup 1.0000x reference)
.LBB0_723:
	s_mov_b32 s0, s9
	s_mov_b32 s8, s1
	v_readlane_b32 s1, v78, s0
	s_add_i32 s1, s1, s8
	s_cmpk_gt_u32 s1, 0xff
	v_sub_co_u32_e64 v79, s[10:11], s0, 1
	s_cselect_b64 s[12:13], -1, 0
	s_or_b64 s[10:11], s[12:13], s[10:11]
	s_andn2_b64 vcc, exec, s[10:11]
	v_readfirstlane_b32 s9, v79
	s_cbranch_vccnz .LBB0_723
	v_readlane_b32 s1, v9, s0
	s_add_i32 s1, s1, s8
	s_cmpk_gt_u32 s1, 0xff
	s_cselect_b64 s[10:11], -1, 0
	s_and_b64 s[10:11], s[10:11], exec
	s_cselect_b32 s14, s8, s1
	v_readlane_b32 s8, v8, s0
	s_add_i32 s15, s14, s8
	s_cmpk_gt_u32 s15, 0xff
	s_cselect_b64 s[8:9], -1, 0
	s_and_b64 s[10:11], s[8:9], exec
	s_cselect_b32 s16, 6, 0
	s_cmpk_gt_u32 s1, 0xff
	s_cselect_b64 s[10:11], -1, 0
	s_and_b64 s[12:13], s[10:11], exec
	s_cselect_b32 s1, 7, s16
	s_or_b64 s[8:9], s[10:11], s[8:9]
	s_and_b64 s[10:11], s[8:9], exec
	s_cselect_b32 s14, s14, s15
	v_readlane_b32 s10, v7, s0
	s_add_i32 s15, s14, s10
	s_cmpk_gt_u32 s15, 0xff
	s_cselect_b64 s[10:11], -1, 0
	s_and_b64 s[12:13], s[10:11], exec
	s_cselect_b32 s16, 5, s1
	s_and_b64 s[12:13], s[8:9], exec
	s_cselect_b32 s1, s1, s16
	s_or_b64 s[8:9], s[8:9], s[10:11]
	s_and_b64 s[10:11], s[8:9], exec
	s_cselect_b32 s14, s14, s15
	v_readlane_b32 s10, v6, s0
	s_add_i32 s15, s14, s10
	s_cmpk_gt_u32 s15, 0xff
	s_cselect_b64 s[10:11], -1, 0
	s_and_b64 s[12:13], s[10:11], exec
	s_cselect_b32 s16, 4, s1
	s_and_b64 s[12:13], s[8:9], exec
	s_cselect_b32 s1, s1, s16
	s_or_b64 s[8:9], s[8:9], s[10:11]
	s_and_b64 s[10:11], s[8:9], exec
	s_cselect_b32 s14, s14, s15
	v_readlane_b32 s10, v5, s0
	s_add_i32 s15, s14, s10
	s_cmpk_gt_u32 s15, 0xff
	s_cselect_b64 s[10:11], -1, 0
	s_and_b64 s[12:13], s[10:11], exec
	s_cselect_b32 s16, 3, s1
	s_and_b64 s[12:13], s[8:9], exec
	s_cselect_b32 s1, s1, s16
	s_or_b64 s[8:9], s[8:9], s[10:11]
	s_and_b64 s[10:11], s[8:9], exec
	s_cselect_b32 s14, s14, s15
	v_readlane_b32 s10, v4, s0
	s_add_i32 s15, s14, s10
	s_cmpk_gt_u32 s15, 0xff
	s_cselect_b64 s[10:11], -1, 0
	s_and_b64 s[12:13], s[10:11], exec
	s_cselect_b32 s16, 2, s1
	s_and_b64 s[12:13], s[8:9], exec
	s_cselect_b32 s1, s1, s16
	s_or_b64 s[8:9], s[8:9], s[10:11]
	s_and_b64 s[10:11], s[8:9], exec
	s_cselect_b32 s14, s14, s15
	v_readlane_b32 s10, v3, s0
	s_add_i32 s15, s14, s10
	s_cmpk_gt_u32 s15, 0xff
	s_cselect_b64 s[10:11], -1, 0
	s_and_b64 s[12:13], s[10:11], exec
	s_cselect_b32 s16, 1, s1
	s_and_b64 s[12:13], s[8:9], exec
	s_cselect_b32 s1, s1, s16
	s_or_b64 s[8:9], s[8:9], s[10:11]
	s_and_b64 s[10:11], s[8:9], exec
	s_cselect_b32 s10, s14, s15
	v_readlane_b32 s11, v2, s0
	s_add_i32 s10, s10, s11
	s_cmpk_lt_u32 s10, 0x100
	s_cselect_b64 s[10:11], -1, 0
	s_or_b64 s[8:9], s[8:9], s[10:11]
	s_and_b64 s[8:9], s[8:9], exec
	s_cselect_b32 s94, s1, 0
	s_lshl_b32 s0, s0, 3
	s_add_i32 s94, s94, s0
	v_readlane_b32 s0, v254, 54
	s_lshl_b32 s22, s94, 7
	v_mov_b32_e32 v91, 0
	v_mov_b32_e32 v7, 0xffff0000
	v_lshl_add_u32 v79, v10, 2, s0
	s_and_b64 vcc, exec, s[60:61]
	s_cbranch_vccz .LBB0_726
	v_cmp_ge_u32_sdwa vcc, v77, s22 src0_sel:WORD_0 src1_sel:DWORD
	s_mov_b32 s0, 0xffff
	v_lshl_or_b32 v2, v77, 16, s0
	v_lshl_add_u32 v5, v91, 8, v79
	ds_write_b32 v5, v2
	v_addc_co_u32_e32 v91, vcc, 0, v91, vcc
	v_cmp_ge_u32_sdwa vcc, v77, s22 src0_sel:WORD_1 src1_sel:DWORD
	s_mov_b32 s1, 0xfffe
	v_and_or_b32 v3, v77, v7, s1
	v_lshl_add_u32 v6, v91, 8, v79
	ds_write_b32 v6, v3
	v_addc_co_u32_e32 v91, vcc, 0, v91, vcc
	v_cmp_ge_u32_sdwa vcc, v76, s22 src0_sel:WORD_0 src1_sel:DWORD
	s_mov_b32 s0, 0xff7f
	v_lshl_or_b32 v4, v76, 16, s0
	v_lshl_add_u32 v5, v91, 8, v79
	ds_write_b32 v5, v4
	v_addc_co_u32_e32 v91, vcc, 0, v91, vcc
	v_cmp_ge_u32_sdwa vcc, v76, s22 src0_sel:WORD_1 src1_sel:DWORD
	s_mov_b32 s1, 0xff7e
	v_and_or_b32 v2, v76, v7, s1
	v_lshl_add_u32 v6, v91, 8, v79
	ds_write_b32 v6, v2
	v_addc_co_u32_e32 v91, vcc, 0, v91, vcc
	v_cmp_ge_u32_sdwa vcc, v75, s22 src0_sel:WORD_0 src1_sel:DWORD
	s_mov_b32 s0, 0xfeff
	v_lshl_or_b32 v3, v75, 16, s0
	v_lshl_add_u32 v5, v91, 8, v79
	ds_write_b32 v5, v3
	v_addc_co_u32_e32 v91, vcc, 0, v91, vcc
	v_cmp_ge_u32_sdwa vcc, v75, s22 src0_sel:WORD_1 src1_sel:DWORD
	s_mov_b32 s1, 0xfefe
	v_and_or_b32 v4, v75, v7, s1
	v_lshl_add_u32 v6, v91, 8, v79
	ds_write_b32 v6, v4
	v_addc_co_u32_e32 v91, vcc, 0, v91, vcc
	v_cmp_ge_u32_sdwa vcc, v74, s22 src0_sel:WORD_0 src1_sel:DWORD
	s_mov_b32 s0, 0xfe7f
	v_lshl_or_b32 v2, v74, 16, s0
	v_lshl_add_u32 v5, v91, 8, v79
	ds_write_b32 v5, v2
	v_addc_co_u32_e32 v91, vcc, 0, v91, vcc
	v_cmp_ge_u32_sdwa vcc, v74, s22 src0_sel:WORD_1 src1_sel:DWORD
	s_mov_b32 s1, 0xfe7e
	v_and_or_b32 v3, v74, v7, s1
	v_lshl_add_u32 v6, v91, 8, v79
	ds_write_b32 v6, v3
	v_addc_co_u32_e32 v91, vcc, 0, v91, vcc
	v_min_u32_e32 v91, 21, v91
	v_cmp_ge_u32_sdwa vcc, v73, s22 src0_sel:WORD_0 src1_sel:DWORD
	s_mov_b32 s0, 0xfdff
	v_lshl_or_b32 v4, v73, 16, s0
	v_lshl_add_u32 v5, v91, 8, v79
	ds_write_b32 v5, v4
	v_addc_co_u32_e32 v91, vcc, 0, v91, vcc
	v_cmp_ge_u32_sdwa vcc, v73, s22 src0_sel:WORD_1 src1_sel:DWORD
	s_mov_b32 s1, 0xfdfe
	v_and_or_b32 v2, v73, v7, s1
	v_lshl_add_u32 v6, v91, 8, v79
	ds_write_b32 v6, v2
	v_addc_co_u32_e32 v91, vcc, 0, v91, vcc
	v_cmp_ge_u32_sdwa vcc, v72, s22 src0_sel:WORD_0 src1_sel:DWORD
	s_mov_b32 s0, 0xfd7f
	v_lshl_or_b32 v3, v72, 16, s0
	v_lshl_add_u32 v5, v91, 8, v79
	ds_write_b32 v5, v3
	v_addc_co_u32_e32 v91, vcc, 0, v91, vcc
	v_cmp_ge_u32_sdwa vcc, v72, s22 src0_sel:WORD_1 src1_sel:DWORD
	s_mov_b32 s1, 0xfd7e
	v_and_or_b32 v4, v72, v7, s1
	v_lshl_add_u32 v6, v91, 8, v79
	ds_write_b32 v6, v4
	v_addc_co_u32_e32 v91, vcc, 0, v91, vcc
	v_cmp_ge_u32_sdwa vcc, v71, s22 src0_sel:WORD_0 src1_sel:DWORD
	s_mov_b32 s0, 0xfcff
	v_lshl_or_b32 v2, v71, 16, s0
	v_lshl_add_u32 v5, v91, 8, v79
	ds_write_b32 v5, v2
	v_addc_co_u32_e32 v91, vcc, 0, v91, vcc
	v_cmp_ge_u32_sdwa vcc, v71, s22 src0_sel:WORD_1 src1_sel:DWORD
	s_mov_b32 s1, 0xfcfe
	v_and_or_b32 v3, v71, v7, s1
	v_lshl_add_u32 v6, v91, 8, v79
	ds_write_b32 v6, v3
	v_addc_co_u32_e32 v91, vcc, 0, v91, vcc
	v_cmp_ge_u32_sdwa vcc, v70, s22 src0_sel:WORD_0 src1_sel:DWORD
	s_mov_b32 s0, 0xfc7f
	v_lshl_or_b32 v4, v70, 16, s0
	v_lshl_add_u32 v5, v91, 8, v79
	ds_write_b32 v5, v4
	v_addc_co_u32_e32 v91, vcc, 0, v91, vcc
	v_cmp_ge_u32_sdwa vcc, v70, s22 src0_sel:WORD_1 src1_sel:DWORD
	s_mov_b32 s1, 0xfc7e
	v_and_or_b32 v2, v70, v7, s1
	v_lshl_add_u32 v6, v91, 8, v79
	ds_write_b32 v6, v2
	v_addc_co_u32_e32 v91, vcc, 0, v91, vcc
	v_min_u32_e32 v91, 21, v91
.LBB0_726:
	v_readlane_b32 s0, v255, 20
	v_readlane_b32 s1, v255, 21
	s_andn2_b64 vcc, exec, s[0:1]
	s_nop 0
	v_cndmask_b32_e64 v2, 0, 1, s[0:1]
	v_cmp_ne_u32_e64 s[8:9], 1, v2
	s_cbranch_vccnz .LBB0_728
	v_cmp_ge_u32_sdwa vcc, v69, s22 src0_sel:WORD_0 src1_sel:DWORD
	s_mov_b32 s0, 0xfbff
	v_lshl_or_b32 v2, v69, 16, s0
	v_lshl_add_u32 v5, v91, 8, v79
	ds_write_b32 v5, v2
	v_addc_co_u32_e32 v91, vcc, 0, v91, vcc
	v_cmp_ge_u32_sdwa vcc, v69, s22 src0_sel:WORD_1 src1_sel:DWORD
	s_mov_b32 s1, 0xfbfe
	v_and_or_b32 v3, v69, v7, s1
	v_lshl_add_u32 v6, v91, 8, v79
	ds_write_b32 v6, v3
	v_addc_co_u32_e32 v91, vcc, 0, v91, vcc
	v_cmp_ge_u32_sdwa vcc, v68, s22 src0_sel:WORD_0 src1_sel:DWORD
	s_mov_b32 s0, 0xfb7f
	v_lshl_or_b32 v4, v68, 16, s0
	v_lshl_add_u32 v5, v91, 8, v79
	ds_write_b32 v5, v4
	v_addc_co_u32_e32 v91, vcc, 0, v91, vcc
	v_cmp_ge_u32_sdwa vcc, v68, s22 src0_sel:WORD_1 src1_sel:DWORD
	s_mov_b32 s1, 0xfb7e
	v_and_or_b32 v2, v68, v7, s1
	v_lshl_add_u32 v6, v91, 8, v79
	ds_write_b32 v6, v2
	v_addc_co_u32_e32 v91, vcc, 0, v91, vcc
	v_cmp_ge_u32_sdwa vcc, v67, s22 src0_sel:WORD_0 src1_sel:DWORD
	s_mov_b32 s0, 0xfaff
	v_lshl_or_b32 v3, v67, 16, s0
	v_lshl_add_u32 v5, v91, 8, v79
	ds_write_b32 v5, v3
	v_addc_co_u32_e32 v91, vcc, 0, v91, vcc
	v_cmp_ge_u32_sdwa vcc, v67, s22 src0_sel:WORD_1 src1_sel:DWORD
	s_mov_b32 s1, 0xfafe
	v_and_or_b32 v4, v67, v7, s1
	v_lshl_add_u32 v6, v91, 8, v79
	ds_write_b32 v6, v4
	v_addc_co_u32_e32 v91, vcc, 0, v91, vcc
	v_cmp_ge_u32_sdwa vcc, v66, s22 src0_sel:WORD_0 src1_sel:DWORD
	s_mov_b32 s0, 0xfa7f
	v_lshl_or_b32 v2, v66, 16, s0
	v_lshl_add_u32 v5, v91, 8, v79
	ds_write_b32 v5, v2
	v_addc_co_u32_e32 v91, vcc, 0, v91, vcc
	v_cmp_ge_u32_sdwa vcc, v66, s22 src0_sel:WORD_1 src1_sel:DWORD
	s_mov_b32 s1, 0xfa7e
	v_and_or_b32 v3, v66, v7, s1
	v_lshl_add_u32 v6, v91, 8, v79
	ds_write_b32 v6, v3
	v_addc_co_u32_e32 v91, vcc, 0, v91, vcc
	v_min_u32_e32 v91, 21, v91
	v_cmp_ge_u32_sdwa vcc, v65, s22 src0_sel:WORD_0 src1_sel:DWORD
	s_mov_b32 s0, 0xf9ff
	v_lshl_or_b32 v4, v65, 16, s0
	v_lshl_add_u32 v5, v91, 8, v79
	ds_write_b32 v5, v4
	v_addc_co_u32_e32 v91, vcc, 0, v91, vcc
	v_cmp_ge_u32_sdwa vcc, v65, s22 src0_sel:WORD_1 src1_sel:DWORD
	s_mov_b32 s1, 0xf9fe
	v_and_or_b32 v2, v65, v7, s1
	v_lshl_add_u32 v6, v91, 8, v79
	ds_write_b32 v6, v2
	v_addc_co_u32_e32 v91, vcc, 0, v91, vcc
	v_cmp_ge_u32_sdwa vcc, v64, s22 src0_sel:WORD_0 src1_sel:DWORD
	s_mov_b32 s0, 0xf97f
	v_lshl_or_b32 v3, v64, 16, s0
	v_lshl_add_u32 v5, v91, 8, v79
	ds_write_b32 v5, v3
	v_addc_co_u32_e32 v91, vcc, 0, v91, vcc
	v_cmp_ge_u32_sdwa vcc, v64, s22 src0_sel:WORD_1 src1_sel:DWORD
	s_mov_b32 s1, 0xf97e
	v_and_or_b32 v4, v64, v7, s1
	v_lshl_add_u32 v6, v91, 8, v79
	ds_write_b32 v6, v4
	v_addc_co_u32_e32 v91, vcc, 0, v91, vcc
	v_cmp_ge_u32_sdwa vcc, v63, s22 src0_sel:WORD_0 src1_sel:DWORD
	s_mov_b32 s0, 0xf8ff
	v_lshl_or_b32 v2, v63, 16, s0
	v_lshl_add_u32 v5, v91, 8, v79
	ds_write_b32 v5, v2
	v_addc_co_u32_e32 v91, vcc, 0, v91, vcc
	v_cmp_ge_u32_sdwa vcc, v63, s22 src0_sel:WORD_1 src1_sel:DWORD
	s_mov_b32 s1, 0xf8fe
	v_and_or_b32 v3, v63, v7, s1
	v_lshl_add_u32 v6, v91, 8, v79
	ds_write_b32 v6, v3
	v_addc_co_u32_e32 v91, vcc, 0, v91, vcc
	v_cmp_ge_u32_sdwa vcc, v62, s22 src0_sel:WORD_0 src1_sel:DWORD
	s_mov_b32 s0, 0xf87f
	v_lshl_or_b32 v4, v62, 16, s0
	v_lshl_add_u32 v5, v91, 8, v79
	ds_write_b32 v5, v4
	v_addc_co_u32_e32 v91, vcc, 0, v91, vcc
	v_cmp_ge_u32_sdwa vcc, v62, s22 src0_sel:WORD_1 src1_sel:DWORD
	s_mov_b32 s1, 0xf87e
	v_and_or_b32 v2, v62, v7, s1
	v_lshl_add_u32 v6, v91, 8, v79
	ds_write_b32 v6, v2
	v_addc_co_u32_e32 v91, vcc, 0, v91, vcc
	v_min_u32_e32 v91, 21, v91
.LBB0_728:
	v_readlane_b32 s0, v255, 22
	v_readlane_b32 s1, v255, 23
	s_andn2_b64 vcc, exec, s[0:1]
	s_nop 0
	v_cndmask_b32_e64 v2, 0, 1, s[0:1]
	v_cmp_ne_u32_e64 s[10:11], 1, v2
	s_cbranch_vccnz .LBB0_730
	v_cmp_ge_u32_sdwa vcc, v61, s22 src0_sel:WORD_0 src1_sel:DWORD
	s_mov_b32 s0, 0xf7ff
	v_lshl_or_b32 v2, v61, 16, s0
	v_lshl_add_u32 v5, v91, 8, v79
	ds_write_b32 v5, v2
	v_addc_co_u32_e32 v91, vcc, 0, v91, vcc
	v_cmp_ge_u32_sdwa vcc, v61, s22 src0_sel:WORD_1 src1_sel:DWORD
	s_mov_b32 s1, 0xf7fe
	v_and_or_b32 v3, v61, v7, s1
	v_lshl_add_u32 v6, v91, 8, v79
	ds_write_b32 v6, v3
	v_addc_co_u32_e32 v91, vcc, 0, v91, vcc
	v_cmp_ge_u32_sdwa vcc, v60, s22 src0_sel:WORD_0 src1_sel:DWORD
	s_mov_b32 s0, 0xf77f
	v_lshl_or_b32 v4, v60, 16, s0
	v_lshl_add_u32 v5, v91, 8, v79
	ds_write_b32 v5, v4
	v_addc_co_u32_e32 v91, vcc, 0, v91, vcc
	v_cmp_ge_u32_sdwa vcc, v60, s22 src0_sel:WORD_1 src1_sel:DWORD
	s_mov_b32 s1, 0xf77e
	v_and_or_b32 v2, v60, v7, s1
	v_lshl_add_u32 v6, v91, 8, v79
	ds_write_b32 v6, v2
	v_addc_co_u32_e32 v91, vcc, 0, v91, vcc
	v_cmp_ge_u32_sdwa vcc, v59, s22 src0_sel:WORD_0 src1_sel:DWORD
	s_mov_b32 s0, 0xf6ff
	v_lshl_or_b32 v3, v59, 16, s0
	v_lshl_add_u32 v5, v91, 8, v79
	ds_write_b32 v5, v3
	v_addc_co_u32_e32 v91, vcc, 0, v91, vcc
	v_cmp_ge_u32_sdwa vcc, v59, s22 src0_sel:WORD_1 src1_sel:DWORD
	s_mov_b32 s1, 0xf6fe
	v_and_or_b32 v4, v59, v7, s1
	v_lshl_add_u32 v6, v91, 8, v79
	ds_write_b32 v6, v4
	v_addc_co_u32_e32 v91, vcc, 0, v91, vcc
	v_cmp_ge_u32_sdwa vcc, v58, s22 src0_sel:WORD_0 src1_sel:DWORD
	s_mov_b32 s0, 0xf67f
	v_lshl_or_b32 v2, v58, 16, s0
	v_lshl_add_u32 v5, v91, 8, v79
	ds_write_b32 v5, v2
	v_addc_co_u32_e32 v91, vcc, 0, v91, vcc
	v_cmp_ge_u32_sdwa vcc, v58, s22 src0_sel:WORD_1 src1_sel:DWORD
	s_mov_b32 s1, 0xf67e
	v_and_or_b32 v3, v58, v7, s1
	v_lshl_add_u32 v6, v91, 8, v79
	ds_write_b32 v6, v3
	v_addc_co_u32_e32 v91, vcc, 0, v91, vcc
	v_min_u32_e32 v91, 21, v91
	v_cmp_ge_u32_sdwa vcc, v57, s22 src0_sel:WORD_0 src1_sel:DWORD
	s_mov_b32 s0, 0xf5ff
	v_lshl_or_b32 v4, v57, 16, s0
	v_lshl_add_u32 v5, v91, 8, v79
	ds_write_b32 v5, v4
	v_addc_co_u32_e32 v91, vcc, 0, v91, vcc
	v_cmp_ge_u32_sdwa vcc, v57, s22 src0_sel:WORD_1 src1_sel:DWORD
	s_mov_b32 s1, 0xf5fe
	v_and_or_b32 v2, v57, v7, s1
	v_lshl_add_u32 v6, v91, 8, v79
	ds_write_b32 v6, v2
	v_addc_co_u32_e32 v91, vcc, 0, v91, vcc
	v_cmp_ge_u32_sdwa vcc, v56, s22 src0_sel:WORD_0 src1_sel:DWORD
	s_mov_b32 s0, 0xf57f
	v_lshl_or_b32 v3, v56, 16, s0
	v_lshl_add_u32 v5, v91, 8, v79
	ds_write_b32 v5, v3
	v_addc_co_u32_e32 v91, vcc, 0, v91, vcc
	v_cmp_ge_u32_sdwa vcc, v56, s22 src0_sel:WORD_1 src1_sel:DWORD
	s_mov_b32 s1, 0xf57e
	v_and_or_b32 v4, v56, v7, s1
	v_lshl_add_u32 v6, v91, 8, v79
	ds_write_b32 v6, v4
	v_addc_co_u32_e32 v91, vcc, 0, v91, vcc
	v_cmp_ge_u32_sdwa vcc, v55, s22 src0_sel:WORD_0 src1_sel:DWORD
	s_mov_b32 s0, 0xf4ff
	v_lshl_or_b32 v2, v55, 16, s0
	v_lshl_add_u32 v5, v91, 8, v79
	ds_write_b32 v5, v2
	v_addc_co_u32_e32 v91, vcc, 0, v91, vcc
	v_cmp_ge_u32_sdwa vcc, v55, s22 src0_sel:WORD_1 src1_sel:DWORD
	s_mov_b32 s1, 0xf4fe
	v_and_or_b32 v3, v55, v7, s1
	v_lshl_add_u32 v6, v91, 8, v79
	ds_write_b32 v6, v3
	v_addc_co_u32_e32 v91, vcc, 0, v91, vcc
	v_cmp_ge_u32_sdwa vcc, v54, s22 src0_sel:WORD_0 src1_sel:DWORD
	s_mov_b32 s0, 0xf47f
	v_lshl_or_b32 v4, v54, 16, s0
	v_lshl_add_u32 v5, v91, 8, v79
	ds_write_b32 v5, v4
	v_addc_co_u32_e32 v91, vcc, 0, v91, vcc
	v_cmp_ge_u32_sdwa vcc, v54, s22 src0_sel:WORD_1 src1_sel:DWORD
	s_mov_b32 s1, 0xf47e
	v_and_or_b32 v2, v54, v7, s1
	v_lshl_add_u32 v6, v91, 8, v79
	ds_write_b32 v6, v2
	v_addc_co_u32_e32 v91, vcc, 0, v91, vcc
	v_min_u32_e32 v91, 21, v91
.LBB0_730:
	v_readlane_b32 s0, v255, 24
	v_readlane_b32 s1, v255, 25
	s_andn2_b64 vcc, exec, s[0:1]
	s_nop 0
	v_cndmask_b32_e64 v2, 0, 1, s[0:1]
	v_cmp_ne_u32_e64 s[12:13], 1, v2
	s_cbranch_vccnz .LBB0_732
	v_cmp_ge_u32_sdwa vcc, v53, s22 src0_sel:WORD_0 src1_sel:DWORD
	s_mov_b32 s0, 0xf3ff
	v_lshl_or_b32 v2, v53, 16, s0
	v_lshl_add_u32 v5, v91, 8, v79
	ds_write_b32 v5, v2
	v_addc_co_u32_e32 v91, vcc, 0, v91, vcc
	v_cmp_ge_u32_sdwa vcc, v53, s22 src0_sel:WORD_1 src1_sel:DWORD
	s_mov_b32 s1, 0xf3fe
	v_and_or_b32 v3, v53, v7, s1
	v_lshl_add_u32 v6, v91, 8, v79
	ds_write_b32 v6, v3
	v_addc_co_u32_e32 v91, vcc, 0, v91, vcc
	v_cmp_ge_u32_sdwa vcc, v52, s22 src0_sel:WORD_0 src1_sel:DWORD
	s_mov_b32 s0, 0xf37f
	v_lshl_or_b32 v4, v52, 16, s0
	v_lshl_add_u32 v5, v91, 8, v79
	ds_write_b32 v5, v4
	v_addc_co_u32_e32 v91, vcc, 0, v91, vcc
	v_cmp_ge_u32_sdwa vcc, v52, s22 src0_sel:WORD_1 src1_sel:DWORD
	s_mov_b32 s1, 0xf37e
	v_and_or_b32 v2, v52, v7, s1
	v_lshl_add_u32 v6, v91, 8, v79
	ds_write_b32 v6, v2
	v_addc_co_u32_e32 v91, vcc, 0, v91, vcc
	v_cmp_ge_u32_sdwa vcc, v51, s22 src0_sel:WORD_0 src1_sel:DWORD
	s_mov_b32 s0, 0xf2ff
	v_lshl_or_b32 v3, v51, 16, s0
	v_lshl_add_u32 v5, v91, 8, v79
	ds_write_b32 v5, v3
	v_addc_co_u32_e32 v91, vcc, 0, v91, vcc
	v_cmp_ge_u32_sdwa vcc, v51, s22 src0_sel:WORD_1 src1_sel:DWORD
	s_mov_b32 s1, 0xf2fe
	v_and_or_b32 v4, v51, v7, s1
	v_lshl_add_u32 v6, v91, 8, v79
	ds_write_b32 v6, v4
	v_addc_co_u32_e32 v91, vcc, 0, v91, vcc
	v_cmp_ge_u32_sdwa vcc, v50, s22 src0_sel:WORD_0 src1_sel:DWORD
	s_mov_b32 s0, 0xf27f
	v_lshl_or_b32 v2, v50, 16, s0
	v_lshl_add_u32 v5, v91, 8, v79
	ds_write_b32 v5, v2
	v_addc_co_u32_e32 v91, vcc, 0, v91, vcc
	v_cmp_ge_u32_sdwa vcc, v50, s22 src0_sel:WORD_1 src1_sel:DWORD
	s_mov_b32 s1, 0xf27e
	v_and_or_b32 v3, v50, v7, s1
	v_lshl_add_u32 v6, v91, 8, v79
	ds_write_b32 v6, v3
	v_addc_co_u32_e32 v91, vcc, 0, v91, vcc
	v_min_u32_e32 v91, 21, v91
	v_cmp_ge_u32_sdwa vcc, v49, s22 src0_sel:WORD_0 src1_sel:DWORD
	s_mov_b32 s0, 0xf1ff
	v_lshl_or_b32 v4, v49, 16, s0
	v_lshl_add_u32 v5, v91, 8, v79
	ds_write_b32 v5, v4
	v_addc_co_u32_e32 v91, vcc, 0, v91, vcc
	v_cmp_ge_u32_sdwa vcc, v49, s22 src0_sel:WORD_1 src1_sel:DWORD
	s_mov_b32 s1, 0xf1fe
	v_and_or_b32 v2, v49, v7, s1
	v_lshl_add_u32 v6, v91, 8, v79
	ds_write_b32 v6, v2
	v_addc_co_u32_e32 v91, vcc, 0, v91, vcc
	v_cmp_ge_u32_sdwa vcc, v48, s22 src0_sel:WORD_0 src1_sel:DWORD
	s_mov_b32 s0, 0xf17f
	v_lshl_or_b32 v3, v48, 16, s0
	v_lshl_add_u32 v5, v91, 8, v79
	ds_write_b32 v5, v3
	v_addc_co_u32_e32 v91, vcc, 0, v91, vcc
	v_cmp_ge_u32_sdwa vcc, v48, s22 src0_sel:WORD_1 src1_sel:DWORD
	s_mov_b32 s1, 0xf17e
	v_and_or_b32 v4, v48, v7, s1
	v_lshl_add_u32 v6, v91, 8, v79
	ds_write_b32 v6, v4
	v_addc_co_u32_e32 v91, vcc, 0, v91, vcc
	v_cmp_ge_u32_sdwa vcc, v47, s22 src0_sel:WORD_0 src1_sel:DWORD
	s_mov_b32 s0, 0xf0ff
	v_lshl_or_b32 v2, v47, 16, s0
	v_lshl_add_u32 v5, v91, 8, v79
	ds_write_b32 v5, v2
	v_addc_co_u32_e32 v91, vcc, 0, v91, vcc
	v_cmp_ge_u32_sdwa vcc, v47, s22 src0_sel:WORD_1 src1_sel:DWORD
	s_mov_b32 s1, 0xf0fe
	v_and_or_b32 v3, v47, v7, s1
	v_lshl_add_u32 v6, v91, 8, v79
	ds_write_b32 v6, v3
	v_addc_co_u32_e32 v91, vcc, 0, v91, vcc
	v_cmp_ge_u32_sdwa vcc, v46, s22 src0_sel:WORD_0 src1_sel:DWORD
	s_mov_b32 s0, 0xf07f
	v_lshl_or_b32 v4, v46, 16, s0
	v_lshl_add_u32 v5, v91, 8, v79
	ds_write_b32 v5, v4
	v_addc_co_u32_e32 v91, vcc, 0, v91, vcc
	v_cmp_ge_u32_sdwa vcc, v46, s22 src0_sel:WORD_1 src1_sel:DWORD
	s_mov_b32 s1, 0xf07e
	v_and_or_b32 v2, v46, v7, s1
	v_lshl_add_u32 v6, v91, 8, v79
	ds_write_b32 v6, v2
	v_addc_co_u32_e32 v91, vcc, 0, v91, vcc
	v_min_u32_e32 v91, 21, v91
.LBB0_732:
	v_readlane_b32 s0, v255, 26
	v_readlane_b32 s1, v255, 27
	s_andn2_b64 vcc, exec, s[0:1]
	s_nop 0
	v_cndmask_b32_e64 v2, 0, 1, s[0:1]
	v_cmp_ne_u32_e64 s[14:15], 1, v2
	s_cbranch_vccnz .LBB0_734
	v_cmp_ge_u32_sdwa vcc, v45, s22 src0_sel:WORD_0 src1_sel:DWORD
	s_mov_b32 s0, 0xefff
	v_lshl_or_b32 v2, v45, 16, s0
	v_lshl_add_u32 v5, v91, 8, v79
	ds_write_b32 v5, v2
	v_addc_co_u32_e32 v91, vcc, 0, v91, vcc
	v_cmp_ge_u32_sdwa vcc, v45, s22 src0_sel:WORD_1 src1_sel:DWORD
	s_mov_b32 s1, 0xeffe
	v_and_or_b32 v3, v45, v7, s1
	v_lshl_add_u32 v6, v91, 8, v79
	ds_write_b32 v6, v3
	v_addc_co_u32_e32 v91, vcc, 0, v91, vcc
	v_cmp_ge_u32_sdwa vcc, v44, s22 src0_sel:WORD_0 src1_sel:DWORD
	s_mov_b32 s0, 0xef7f
	v_lshl_or_b32 v4, v44, 16, s0
	v_lshl_add_u32 v5, v91, 8, v79
	ds_write_b32 v5, v4
	v_addc_co_u32_e32 v91, vcc, 0, v91, vcc
	v_cmp_ge_u32_sdwa vcc, v44, s22 src0_sel:WORD_1 src1_sel:DWORD
	s_mov_b32 s1, 0xef7e
	v_and_or_b32 v2, v44, v7, s1
	v_lshl_add_u32 v6, v91, 8, v79
	ds_write_b32 v6, v2
	v_addc_co_u32_e32 v91, vcc, 0, v91, vcc
	v_cmp_ge_u32_sdwa vcc, v43, s22 src0_sel:WORD_0 src1_sel:DWORD
	s_mov_b32 s0, 0xeeff
	v_lshl_or_b32 v3, v43, 16, s0
	v_lshl_add_u32 v5, v91, 8, v79
	ds_write_b32 v5, v3
	v_addc_co_u32_e32 v91, vcc, 0, v91, vcc
	v_cmp_ge_u32_sdwa vcc, v43, s22 src0_sel:WORD_1 src1_sel:DWORD
	s_mov_b32 s1, 0xeefe
	v_and_or_b32 v4, v43, v7, s1
	v_lshl_add_u32 v6, v91, 8, v79
	ds_write_b32 v6, v4
	v_addc_co_u32_e32 v91, vcc, 0, v91, vcc
	v_cmp_ge_u32_sdwa vcc, v42, s22 src0_sel:WORD_0 src1_sel:DWORD
	s_mov_b32 s0, 0xee7f
	v_lshl_or_b32 v2, v42, 16, s0
	v_lshl_add_u32 v5, v91, 8, v79
	ds_write_b32 v5, v2
	v_addc_co_u32_e32 v91, vcc, 0, v91, vcc
	v_cmp_ge_u32_sdwa vcc, v42, s22 src0_sel:WORD_1 src1_sel:DWORD
	s_mov_b32 s1, 0xee7e
	v_and_or_b32 v3, v42, v7, s1
	v_lshl_add_u32 v6, v91, 8, v79
	ds_write_b32 v6, v3
	v_addc_co_u32_e32 v91, vcc, 0, v91, vcc
	v_min_u32_e32 v91, 21, v91
	v_cmp_ge_u32_sdwa vcc, v41, s22 src0_sel:WORD_0 src1_sel:DWORD
	s_mov_b32 s0, 0xedff
	v_lshl_or_b32 v4, v41, 16, s0
	v_lshl_add_u32 v5, v91, 8, v79
	ds_write_b32 v5, v4
	v_addc_co_u32_e32 v91, vcc, 0, v91, vcc
	v_cmp_ge_u32_sdwa vcc, v41, s22 src0_sel:WORD_1 src1_sel:DWORD
	s_mov_b32 s1, 0xedfe
	v_and_or_b32 v2, v41, v7, s1
	v_lshl_add_u32 v6, v91, 8, v79
	ds_write_b32 v6, v2
	v_addc_co_u32_e32 v91, vcc, 0, v91, vcc
	v_cmp_ge_u32_sdwa vcc, v40, s22 src0_sel:WORD_0 src1_sel:DWORD
	s_mov_b32 s0, 0xed7f
	v_lshl_or_b32 v3, v40, 16, s0
	v_lshl_add_u32 v5, v91, 8, v79
	ds_write_b32 v5, v3
	v_addc_co_u32_e32 v91, vcc, 0, v91, vcc
	v_cmp_ge_u32_sdwa vcc, v40, s22 src0_sel:WORD_1 src1_sel:DWORD
	s_mov_b32 s1, 0xed7e
	v_and_or_b32 v4, v40, v7, s1
	v_lshl_add_u32 v6, v91, 8, v79
	ds_write_b32 v6, v4
	v_addc_co_u32_e32 v91, vcc, 0, v91, vcc
	v_cmp_ge_u32_sdwa vcc, v39, s22 src0_sel:WORD_0 src1_sel:DWORD
	s_mov_b32 s0, 0xecff
	v_lshl_or_b32 v2, v39, 16, s0
	v_lshl_add_u32 v5, v91, 8, v79
	ds_write_b32 v5, v2
	v_addc_co_u32_e32 v91, vcc, 0, v91, vcc
	v_cmp_ge_u32_sdwa vcc, v39, s22 src0_sel:WORD_1 src1_sel:DWORD
	s_mov_b32 s1, 0xecfe
	v_and_or_b32 v3, v39, v7, s1
	v_lshl_add_u32 v6, v91, 8, v79
	ds_write_b32 v6, v3
	v_addc_co_u32_e32 v91, vcc, 0, v91, vcc
	v_cmp_ge_u32_sdwa vcc, v38, s22 src0_sel:WORD_0 src1_sel:DWORD
	s_mov_b32 s0, 0xec7f
	v_lshl_or_b32 v4, v38, 16, s0
	v_lshl_add_u32 v5, v91, 8, v79
	ds_write_b32 v5, v4
	v_addc_co_u32_e32 v91, vcc, 0, v91, vcc
	v_cmp_ge_u32_sdwa vcc, v38, s22 src0_sel:WORD_1 src1_sel:DWORD
	s_mov_b32 s1, 0xec7e
	v_and_or_b32 v2, v38, v7, s1
	v_lshl_add_u32 v6, v91, 8, v79
	ds_write_b32 v6, v2
	v_addc_co_u32_e32 v91, vcc, 0, v91, vcc
	v_min_u32_e32 v91, 21, v91
.LBB0_734:
	v_readlane_b32 s0, v255, 28
	v_readlane_b32 s1, v255, 29
	s_andn2_b64 vcc, exec, s[0:1]
	s_nop 0
	v_cndmask_b32_e64 v2, 0, 1, s[0:1]
	v_cmp_ne_u32_e64 s[16:17], 1, v2
	s_cbranch_vccnz .LBB0_736
	v_cmp_ge_u32_sdwa vcc, v37, s22 src0_sel:WORD_0 src1_sel:DWORD
	s_mov_b32 s0, 0xebff
	v_lshl_or_b32 v2, v37, 16, s0
	v_lshl_add_u32 v5, v91, 8, v79
	ds_write_b32 v5, v2
	v_addc_co_u32_e32 v91, vcc, 0, v91, vcc
	v_cmp_ge_u32_sdwa vcc, v37, s22 src0_sel:WORD_1 src1_sel:DWORD
	s_mov_b32 s1, 0xebfe
	v_and_or_b32 v3, v37, v7, s1
	v_lshl_add_u32 v6, v91, 8, v79
	ds_write_b32 v6, v3
	v_addc_co_u32_e32 v91, vcc, 0, v91, vcc
	v_cmp_ge_u32_sdwa vcc, v36, s22 src0_sel:WORD_0 src1_sel:DWORD
	s_mov_b32 s0, 0xeb7f
	v_lshl_or_b32 v4, v36, 16, s0
	v_lshl_add_u32 v5, v91, 8, v79
	ds_write_b32 v5, v4
	v_addc_co_u32_e32 v91, vcc, 0, v91, vcc
	v_cmp_ge_u32_sdwa vcc, v36, s22 src0_sel:WORD_1 src1_sel:DWORD
	s_mov_b32 s1, 0xeb7e
	v_and_or_b32 v2, v36, v7, s1
	v_lshl_add_u32 v6, v91, 8, v79
	ds_write_b32 v6, v2
	v_addc_co_u32_e32 v91, vcc, 0, v91, vcc
	v_cmp_ge_u32_sdwa vcc, v35, s22 src0_sel:WORD_0 src1_sel:DWORD
	s_mov_b32 s0, 0xeaff
	v_lshl_or_b32 v3, v35, 16, s0
	v_lshl_add_u32 v5, v91, 8, v79
	ds_write_b32 v5, v3
	v_addc_co_u32_e32 v91, vcc, 0, v91, vcc
	v_cmp_ge_u32_sdwa vcc, v35, s22 src0_sel:WORD_1 src1_sel:DWORD
	s_mov_b32 s1, 0xeafe
	v_and_or_b32 v4, v35, v7, s1
	v_lshl_add_u32 v6, v91, 8, v79
	ds_write_b32 v6, v4
	v_addc_co_u32_e32 v91, vcc, 0, v91, vcc
	v_cmp_ge_u32_sdwa vcc, v34, s22 src0_sel:WORD_0 src1_sel:DWORD
	s_mov_b32 s0, 0xea7f
	v_lshl_or_b32 v2, v34, 16, s0
	v_lshl_add_u32 v5, v91, 8, v79
	ds_write_b32 v5, v2
	v_addc_co_u32_e32 v91, vcc, 0, v91, vcc
	v_cmp_ge_u32_sdwa vcc, v34, s22 src0_sel:WORD_1 src1_sel:DWORD
	s_mov_b32 s1, 0xea7e
	v_and_or_b32 v3, v34, v7, s1
	v_lshl_add_u32 v6, v91, 8, v79
	ds_write_b32 v6, v3
	v_addc_co_u32_e32 v91, vcc, 0, v91, vcc
	v_min_u32_e32 v91, 21, v91
	v_cmp_ge_u32_sdwa vcc, v33, s22 src0_sel:WORD_0 src1_sel:DWORD
	s_mov_b32 s0, 0xe9ff
	v_lshl_or_b32 v4, v33, 16, s0
	v_lshl_add_u32 v5, v91, 8, v79
	ds_write_b32 v5, v4
	v_addc_co_u32_e32 v91, vcc, 0, v91, vcc
	v_cmp_ge_u32_sdwa vcc, v33, s22 src0_sel:WORD_1 src1_sel:DWORD
	s_mov_b32 s1, 0xe9fe
	v_and_or_b32 v2, v33, v7, s1
	v_lshl_add_u32 v6, v91, 8, v79
	ds_write_b32 v6, v2
	v_addc_co_u32_e32 v91, vcc, 0, v91, vcc
	v_cmp_ge_u32_sdwa vcc, v32, s22 src0_sel:WORD_0 src1_sel:DWORD
	s_mov_b32 s0, 0xe97f
	v_lshl_or_b32 v3, v32, 16, s0
	v_lshl_add_u32 v5, v91, 8, v79
	ds_write_b32 v5, v3
	v_addc_co_u32_e32 v91, vcc, 0, v91, vcc
	v_cmp_ge_u32_sdwa vcc, v32, s22 src0_sel:WORD_1 src1_sel:DWORD
	s_mov_b32 s1, 0xe97e
	v_and_or_b32 v4, v32, v7, s1
	v_lshl_add_u32 v6, v91, 8, v79
	ds_write_b32 v6, v4
	v_addc_co_u32_e32 v91, vcc, 0, v91, vcc
	v_cmp_ge_u32_sdwa vcc, v31, s22 src0_sel:WORD_0 src1_sel:DWORD
	s_mov_b32 s0, 0xe8ff
	v_lshl_or_b32 v2, v31, 16, s0
	v_lshl_add_u32 v5, v91, 8, v79
	ds_write_b32 v5, v2
	v_addc_co_u32_e32 v91, vcc, 0, v91, vcc
	v_cmp_ge_u32_sdwa vcc, v31, s22 src0_sel:WORD_1 src1_sel:DWORD
	s_mov_b32 s1, 0xe8fe
	v_and_or_b32 v3, v31, v7, s1
	v_lshl_add_u32 v6, v91, 8, v79
	ds_write_b32 v6, v3
	v_addc_co_u32_e32 v91, vcc, 0, v91, vcc
	v_cmp_ge_u32_sdwa vcc, v30, s22 src0_sel:WORD_0 src1_sel:DWORD
	s_mov_b32 s0, 0xe87f
	v_lshl_or_b32 v4, v30, 16, s0
	v_lshl_add_u32 v5, v91, 8, v79
	ds_write_b32 v5, v4
	v_addc_co_u32_e32 v91, vcc, 0, v91, vcc
	v_cmp_ge_u32_sdwa vcc, v30, s22 src0_sel:WORD_1 src1_sel:DWORD
	s_mov_b32 s1, 0xe87e
	v_and_or_b32 v2, v30, v7, s1
	v_lshl_add_u32 v6, v91, 8, v79
	ds_write_b32 v6, v2
	v_addc_co_u32_e32 v91, vcc, 0, v91, vcc
	v_min_u32_e32 v91, 21, v91
.LBB0_736:
	v_readlane_b32 s0, v255, 30
	v_readlane_b32 s1, v255, 31
	s_andn2_b64 vcc, exec, s[0:1]
	s_nop 0
	v_cndmask_b32_e64 v2, 0, 1, s[0:1]
	v_cmp_ne_u32_e64 s[18:19], 1, v2
	s_cbranch_vccnz .LBB0_738
	v_cmp_ge_u32_sdwa vcc, v29, s22 src0_sel:WORD_0 src1_sel:DWORD
	s_mov_b32 s0, 0xe7ff
	v_lshl_or_b32 v2, v29, 16, s0
	v_lshl_add_u32 v5, v91, 8, v79
	ds_write_b32 v5, v2
	v_addc_co_u32_e32 v91, vcc, 0, v91, vcc
	v_cmp_ge_u32_sdwa vcc, v29, s22 src0_sel:WORD_1 src1_sel:DWORD
	s_mov_b32 s1, 0xe7fe
	v_and_or_b32 v3, v29, v7, s1
	v_lshl_add_u32 v6, v91, 8, v79
	ds_write_b32 v6, v3
	v_addc_co_u32_e32 v91, vcc, 0, v91, vcc
	v_cmp_ge_u32_sdwa vcc, v28, s22 src0_sel:WORD_0 src1_sel:DWORD
	s_mov_b32 s0, 0xe77f
	v_lshl_or_b32 v4, v28, 16, s0
	v_lshl_add_u32 v5, v91, 8, v79
	ds_write_b32 v5, v4
	v_addc_co_u32_e32 v91, vcc, 0, v91, vcc
	v_cmp_ge_u32_sdwa vcc, v28, s22 src0_sel:WORD_1 src1_sel:DWORD
	s_mov_b32 s1, 0xe77e
	v_and_or_b32 v2, v28, v7, s1
	v_lshl_add_u32 v6, v91, 8, v79
	ds_write_b32 v6, v2
	v_addc_co_u32_e32 v91, vcc, 0, v91, vcc
	v_cmp_ge_u32_sdwa vcc, v27, s22 src0_sel:WORD_0 src1_sel:DWORD
	s_mov_b32 s0, 0xe6ff
	v_lshl_or_b32 v3, v27, 16, s0
	v_lshl_add_u32 v5, v91, 8, v79
	ds_write_b32 v5, v3
	v_addc_co_u32_e32 v91, vcc, 0, v91, vcc
	v_cmp_ge_u32_sdwa vcc, v27, s22 src0_sel:WORD_1 src1_sel:DWORD
	s_mov_b32 s1, 0xe6fe
	v_and_or_b32 v4, v27, v7, s1
	v_lshl_add_u32 v6, v91, 8, v79
	ds_write_b32 v6, v4
	v_addc_co_u32_e32 v91, vcc, 0, v91, vcc
	v_cmp_ge_u32_sdwa vcc, v26, s22 src0_sel:WORD_0 src1_sel:DWORD
	s_mov_b32 s0, 0xe67f
	v_lshl_or_b32 v2, v26, 16, s0
	v_lshl_add_u32 v5, v91, 8, v79
	ds_write_b32 v5, v2
	v_addc_co_u32_e32 v91, vcc, 0, v91, vcc
	v_cmp_ge_u32_sdwa vcc, v26, s22 src0_sel:WORD_1 src1_sel:DWORD
	s_mov_b32 s1, 0xe67e
	v_and_or_b32 v3, v26, v7, s1
	v_lshl_add_u32 v6, v91, 8, v79
	ds_write_b32 v6, v3
	v_addc_co_u32_e32 v91, vcc, 0, v91, vcc
	v_min_u32_e32 v91, 21, v91
	v_cmp_ge_u32_sdwa vcc, v25, s22 src0_sel:WORD_0 src1_sel:DWORD
	s_mov_b32 s0, 0xe5ff
	v_lshl_or_b32 v4, v25, 16, s0
	v_lshl_add_u32 v5, v91, 8, v79
	ds_write_b32 v5, v4
	v_addc_co_u32_e32 v91, vcc, 0, v91, vcc
	v_cmp_ge_u32_sdwa vcc, v25, s22 src0_sel:WORD_1 src1_sel:DWORD
	s_mov_b32 s1, 0xe5fe
	v_and_or_b32 v2, v25, v7, s1
	v_lshl_add_u32 v6, v91, 8, v79
	ds_write_b32 v6, v2
	v_addc_co_u32_e32 v91, vcc, 0, v91, vcc
	v_cmp_ge_u32_sdwa vcc, v24, s22 src0_sel:WORD_0 src1_sel:DWORD
	s_mov_b32 s0, 0xe57f
	v_lshl_or_b32 v3, v24, 16, s0
	v_lshl_add_u32 v5, v91, 8, v79
	ds_write_b32 v5, v3
	v_addc_co_u32_e32 v91, vcc, 0, v91, vcc
	v_cmp_ge_u32_sdwa vcc, v24, s22 src0_sel:WORD_1 src1_sel:DWORD
	s_mov_b32 s1, 0xe57e
	v_and_or_b32 v4, v24, v7, s1
	v_lshl_add_u32 v6, v91, 8, v79
	ds_write_b32 v6, v4
	v_addc_co_u32_e32 v91, vcc, 0, v91, vcc
	v_cmp_ge_u32_sdwa vcc, v23, s22 src0_sel:WORD_0 src1_sel:DWORD
	s_mov_b32 s0, 0xe4ff
	v_lshl_or_b32 v2, v23, 16, s0
	v_lshl_add_u32 v5, v91, 8, v79
	ds_write_b32 v5, v2
	v_addc_co_u32_e32 v91, vcc, 0, v91, vcc
	v_cmp_ge_u32_sdwa vcc, v23, s22 src0_sel:WORD_1 src1_sel:DWORD
	s_mov_b32 s1, 0xe4fe
	v_and_or_b32 v3, v23, v7, s1
	v_lshl_add_u32 v6, v91, 8, v79
	ds_write_b32 v6, v3
	v_addc_co_u32_e32 v91, vcc, 0, v91, vcc
	v_cmp_ge_u32_sdwa vcc, v22, s22 src0_sel:WORD_0 src1_sel:DWORD
	s_mov_b32 s0, 0xe47f
	v_lshl_or_b32 v4, v22, 16, s0
	v_lshl_add_u32 v5, v91, 8, v79
	ds_write_b32 v5, v4
	v_addc_co_u32_e32 v91, vcc, 0, v91, vcc
	v_cmp_ge_u32_sdwa vcc, v22, s22 src0_sel:WORD_1 src1_sel:DWORD
	s_mov_b32 s1, 0xe47e
	v_and_or_b32 v2, v22, v7, s1
	v_lshl_add_u32 v6, v91, 8, v79
	ds_write_b32 v6, v2
	v_addc_co_u32_e32 v91, vcc, 0, v91, vcc
	v_min_u32_e32 v91, 21, v91
.LBB0_738:
	v_readlane_b32 s0, v255, 32
	v_readlane_b32 s1, v255, 33
	s_andn2_b64 vcc, exec, s[0:1]
	s_nop 0
	v_cndmask_b32_e64 v2, 0, 1, s[0:1]
	v_cmp_ne_u32_e64 s[20:21], 1, v2
	s_cbranch_vccnz .LBB0_740
	v_cmp_ge_u32_sdwa vcc, v21, s22 src0_sel:WORD_0 src1_sel:DWORD
	s_mov_b32 s0, 0xe3ff
	v_lshl_or_b32 v2, v21, 16, s0
	v_lshl_add_u32 v5, v91, 8, v79
	ds_write_b32 v5, v2
	v_addc_co_u32_e32 v91, vcc, 0, v91, vcc
	v_cmp_ge_u32_sdwa vcc, v21, s22 src0_sel:WORD_1 src1_sel:DWORD
	s_mov_b32 s1, 0xe3fe
	v_and_or_b32 v3, v21, v7, s1
	v_lshl_add_u32 v6, v91, 8, v79
	ds_write_b32 v6, v3
	v_addc_co_u32_e32 v91, vcc, 0, v91, vcc
	v_cmp_ge_u32_sdwa vcc, v20, s22 src0_sel:WORD_0 src1_sel:DWORD
	s_mov_b32 s0, 0xe37f
	v_lshl_or_b32 v4, v20, 16, s0
	v_lshl_add_u32 v5, v91, 8, v79
	ds_write_b32 v5, v4
	v_addc_co_u32_e32 v91, vcc, 0, v91, vcc
	v_cmp_ge_u32_sdwa vcc, v20, s22 src0_sel:WORD_1 src1_sel:DWORD
	s_mov_b32 s1, 0xe37e
	v_and_or_b32 v2, v20, v7, s1
	v_lshl_add_u32 v6, v91, 8, v79
	ds_write_b32 v6, v2
	v_addc_co_u32_e32 v91, vcc, 0, v91, vcc
	v_cmp_ge_u32_sdwa vcc, v19, s22 src0_sel:WORD_0 src1_sel:DWORD
	s_mov_b32 s0, 0xe2ff
	v_lshl_or_b32 v3, v19, 16, s0
	v_lshl_add_u32 v5, v91, 8, v79
	ds_write_b32 v5, v3
	v_addc_co_u32_e32 v91, vcc, 0, v91, vcc
	v_cmp_ge_u32_sdwa vcc, v19, s22 src0_sel:WORD_1 src1_sel:DWORD
	s_mov_b32 s1, 0xe2fe
	v_and_or_b32 v4, v19, v7, s1
	v_lshl_add_u32 v6, v91, 8, v79
	ds_write_b32 v6, v4
	v_addc_co_u32_e32 v91, vcc, 0, v91, vcc
	v_cmp_ge_u32_sdwa vcc, v18, s22 src0_sel:WORD_0 src1_sel:DWORD
	s_mov_b32 s0, 0xe27f
	v_lshl_or_b32 v2, v18, 16, s0
	v_lshl_add_u32 v5, v91, 8, v79
	ds_write_b32 v5, v2
	v_addc_co_u32_e32 v91, vcc, 0, v91, vcc
	v_cmp_ge_u32_sdwa vcc, v18, s22 src0_sel:WORD_1 src1_sel:DWORD
	s_mov_b32 s1, 0xe27e
	v_and_or_b32 v3, v18, v7, s1
	v_lshl_add_u32 v6, v91, 8, v79
	ds_write_b32 v6, v3
	v_addc_co_u32_e32 v91, vcc, 0, v91, vcc
	v_min_u32_e32 v91, 21, v91
	v_cmp_ge_u32_sdwa vcc, v17, s22 src0_sel:WORD_0 src1_sel:DWORD
	s_mov_b32 s0, 0xe1ff
	v_lshl_or_b32 v4, v17, 16, s0
	v_lshl_add_u32 v5, v91, 8, v79
	ds_write_b32 v5, v4
	v_addc_co_u32_e32 v91, vcc, 0, v91, vcc
	v_cmp_ge_u32_sdwa vcc, v17, s22 src0_sel:WORD_1 src1_sel:DWORD
	s_mov_b32 s1, 0xe1fe
	v_and_or_b32 v2, v17, v7, s1
	v_lshl_add_u32 v6, v91, 8, v79
	ds_write_b32 v6, v2
	v_addc_co_u32_e32 v91, vcc, 0, v91, vcc
	v_cmp_ge_u32_sdwa vcc, v16, s22 src0_sel:WORD_0 src1_sel:DWORD
	s_mov_b32 s0, 0xe17f
	v_lshl_or_b32 v3, v16, 16, s0
	v_lshl_add_u32 v5, v91, 8, v79
	ds_write_b32 v5, v3
	v_addc_co_u32_e32 v91, vcc, 0, v91, vcc
	v_cmp_ge_u32_sdwa vcc, v16, s22 src0_sel:WORD_1 src1_sel:DWORD
	s_mov_b32 s1, 0xe17e
	v_and_or_b32 v4, v16, v7, s1
	v_lshl_add_u32 v6, v91, 8, v79
	ds_write_b32 v6, v4
	v_addc_co_u32_e32 v91, vcc, 0, v91, vcc
	v_cmp_ge_u32_sdwa vcc, v15, s22 src0_sel:WORD_0 src1_sel:DWORD
	s_mov_b32 s0, 0xe0ff
	v_lshl_or_b32 v2, v15, 16, s0
	v_lshl_add_u32 v5, v91, 8, v79
	ds_write_b32 v5, v2
	v_addc_co_u32_e32 v91, vcc, 0, v91, vcc
	v_cmp_ge_u32_sdwa vcc, v15, s22 src0_sel:WORD_1 src1_sel:DWORD
	s_mov_b32 s1, 0xe0fe
	v_and_or_b32 v3, v15, v7, s1
	v_lshl_add_u32 v6, v91, 8, v79
	ds_write_b32 v6, v3
	v_addc_co_u32_e32 v91, vcc, 0, v91, vcc
	v_cmp_ge_u32_sdwa vcc, v14, s22 src0_sel:WORD_0 src1_sel:DWORD
	s_mov_b32 s0, 0xe07f
	v_lshl_or_b32 v4, v14, 16, s0
	v_lshl_add_u32 v5, v91, 8, v79
	ds_write_b32 v5, v4
	v_addc_co_u32_e32 v91, vcc, 0, v91, vcc
	v_cmp_ge_u32_sdwa vcc, v14, s22 src0_sel:WORD_1 src1_sel:DWORD
	s_mov_b32 s1, 0xe07e
	v_and_or_b32 v2, v14, v7, s1
	v_lshl_add_u32 v6, v91, 8, v79
	ds_write_b32 v6, v2
	v_addc_co_u32_e32 v91, vcc, 0, v91, vcc
	v_min_u32_e32 v91, 21, v91

.LBB0_777:
	s_mov_b64 s[0:1], 0
	s_cbranch_execz .LBB0_921
	s_waitcnt lgkmcnt(0)
	v_mov_b32_e32 v88, 0
	v_cmp_ne_u32_e32 vcc, 0, v91
	v_mov_b32_e32 v90, 0
	s_and_saveexec_b64 s[0:1], vcc
	ds_read_b32 v90, v79
	s_or_b64 exec, exec, s[0:1]
	v_cndmask_b32_e64 v2, 0, 1, vcc
	v_cmp_ne_u32_e32 vcc, 0, v2
	v_cmp_lt_u32_e64 s[0:1], 1, v91
	s_and_saveexec_b64 s[8:9], s[0:1]
	ds_read_b32 v88, v79 offset:256
	s_or_b64 exec, exec, s[8:9]
	v_cndmask_b32_e64 v2, 0, 1, s[0:1]
	v_mov_b32_e32 v86, 0
	v_cmp_ne_u32_e64 s[8:9], 0, v2
	v_cmp_lt_u32_e64 s[0:1], 2, v91
	v_mov_b32_e32 v89, 0
	s_and_saveexec_b64 s[10:11], s[0:1]
	ds_read_b32 v89, v79 offset:512
	s_or_b64 exec, exec, s[10:11]
	v_cndmask_b32_e64 v2, 0, 1, s[0:1]
	v_cmp_ne_u32_e64 s[10:11], 0, v2
	v_cmp_lt_u32_e64 s[0:1], 3, v91
	s_and_saveexec_b64 s[12:13], s[0:1]
	ds_read_b32 v86, v79 offset:768
	s_or_b64 exec, exec, s[12:13]
	v_cndmask_b32_e64 v2, 0, 1, s[0:1]
	v_mov_b32_e32 v84, 0
	v_cmp_ne_u32_e64 s[12:13], 0, v2
	v_cmp_lt_u32_e64 s[0:1], 4, v91
	v_mov_b32_e32 v87, 0
	s_and_saveexec_b64 s[14:15], s[0:1]
	ds_read_b32 v87, v79 offset:1024
	s_or_b64 exec, exec, s[14:15]
	v_cndmask_b32_e64 v2, 0, 1, s[0:1]
	v_cmp_ne_u32_e64 s[14:15], 0, v2
	v_cmp_lt_u32_e64 s[0:1], 5, v91
	s_and_saveexec_b64 s[16:17], s[0:1]
	ds_read_b32 v84, v79 offset:1280
	s_or_b64 exec, exec, s[16:17]
	v_cndmask_b32_e64 v2, 0, 1, s[0:1]
	v_mov_b32_e32 v82, 0
	v_cmp_ne_u32_e64 s[16:17], 0, v2
	v_cmp_lt_u32_e64 s[0:1], 6, v91
	v_mov_b32_e32 v85, 0
	s_and_saveexec_b64 s[18:19], s[0:1]
	ds_read_b32 v85, v79 offset:1536
	s_or_b64 exec, exec, s[18:19]
	v_cndmask_b32_e64 v2, 0, 1, s[0:1]
	v_cmp_ne_u32_e64 s[18:19], 0, v2
	v_cmp_lt_u32_e64 s[0:1], 7, v91
	s_and_saveexec_b64 s[20:21], s[0:1]
	ds_read_b32 v82, v79 offset:1792
	s_or_b64 exec, exec, s[20:21]
	v_cndmask_b32_e64 v2, 0, 1, s[0:1]
	v_mov_b32_e32 v80, 0
	v_cmp_ne_u32_e64 s[20:21], 0, v2
	v_cmp_lt_u32_e64 s[0:1], 8, v91
	v_mov_b32_e32 v83, 0
	s_and_saveexec_b64 s[22:23], s[0:1]
	ds_read_b32 v83, v79 offset:2048
	s_or_b64 exec, exec, s[22:23]
	v_cndmask_b32_e64 v2, 0, 1, s[0:1]
	v_cmp_ne_u32_e64 s[22:23], 0, v2
	v_cmp_lt_u32_e64 s[0:1], 9, v91
	s_and_saveexec_b64 s[24:25], s[0:1]
	ds_read_b32 v80, v79 offset:2304
	s_or_b64 exec, exec, s[24:25]
	v_cndmask_b32_e64 v2, 0, 1, s[0:1]
	v_mov_b32_e32 v9, 0
	v_cmp_ne_u32_e64 s[24:25], 0, v2
	v_cmp_lt_u32_e64 s[0:1], 10, v91
	v_mov_b32_e32 v81, 0
	s_and_saveexec_b64 s[26:27], s[0:1]
	ds_read_b32 v81, v79 offset:2560
	s_or_b64 exec, exec, s[26:27]
	v_cndmask_b32_e64 v2, 0, 1, s[0:1]
	v_cmp_ne_u32_e64 s[26:27], 0, v2
	v_cmp_lt_u32_e64 s[0:1], 11, v91
	s_and_saveexec_b64 s[28:29], s[0:1]
	ds_read_b32 v9, v79 offset:2816
	s_or_b64 exec, exec, s[28:29]
	v_cndmask_b32_e64 v2, 0, 1, s[0:1]
	v_mov_b32_e32 v7, 0
	v_cmp_ne_u32_e64 s[28:29], 0, v2
	v_cmp_lt_u32_e64 s[0:1], 12, v91
	v_mov_b32_e32 v78, 0
	s_and_saveexec_b64 s[30:31], s[0:1]
	ds_read_b32 v78, v79 offset:3072
	s_or_b64 exec, exec, s[30:31]
	v_cndmask_b32_e64 v2, 0, 1, s[0:1]
	v_cmp_ne_u32_e64 s[30:31], 0, v2
	v_cmp_lt_u32_e64 s[0:1], 13, v91
	s_and_saveexec_b64 s[34:35], s[0:1]
	ds_read_b32 v7, v79 offset:3328
	s_or_b64 exec, exec, s[34:35]
	v_cndmask_b32_e64 v2, 0, 1, s[0:1]
	v_mov_b32_e32 v5, 0
	v_cmp_ne_u32_e64 s[34:35], 0, v2
	v_cmp_lt_u32_e64 s[0:1], 14, v91
	v_mov_b32_e32 v8, 0
	s_and_saveexec_b64 s[36:37], s[0:1]
	ds_read_b32 v8, v79 offset:3584
	s_or_b64 exec, exec, s[36:37]
	v_cndmask_b32_e64 v2, 0, 1, s[0:1]
	v_cmp_ne_u32_e64 s[36:37], 0, v2
	v_cmp_lt_u32_e64 s[0:1], 15, v91
	s_and_saveexec_b64 s[38:39], s[0:1]
	ds_read_b32 v5, v79 offset:3840
	s_or_b64 exec, exec, s[38:39]
	v_cndmask_b32_e64 v2, 0, 1, s[0:1]
	v_mov_b32_e32 v3, 0
	v_cmp_ne_u32_e64 s[38:39], 0, v2
	v_cmp_lt_u32_e64 s[0:1], 16, v91
	v_mov_b32_e32 v6, 0
	s_and_saveexec_b64 s[40:41], s[0:1]
	ds_read_b32 v6, v79 offset:4096
	s_or_b64 exec, exec, s[40:41]
	v_cndmask_b32_e64 v2, 0, 1, s[0:1]
	v_cmp_ne_u32_e64 s[40:41], 0, v2
	v_cmp_lt_u32_e64 s[0:1], 17, v91
	s_and_saveexec_b64 s[42:43], s[0:1]
	ds_read_b32 v3, v79 offset:4352
	s_or_b64 exec, exec, s[42:43]
	v_cndmask_b32_e64 v4, 0, 1, s[0:1]
	v_mov_b32_e32 v2, 0
	v_cmp_ne_u32_e64 s[42:43], 0, v4
	v_cmp_lt_u32_e64 s[0:1], 18, v91
	v_mov_b32_e32 v4, 0
	s_and_saveexec_b64 s[46:47], s[0:1]
	ds_read_b32 v4, v79 offset:4608
	s_or_b64 exec, exec, s[46:47]
	v_cndmask_b32_e64 v92, 0, 1, s[0:1]
	v_cmp_ne_u32_e64 s[46:47], 0, v92
	v_cmp_lt_u32_e64 s[0:1], 19, v91
	s_and_saveexec_b64 s[78:79], s[0:1]
	ds_read_b32 v2, v79 offset:4864
	s_or_b64 exec, exec, s[78:79]
	s_cmp_lg_u64 vcc, 0
	s_cselect_b64 s[78:79], -1, 0
	v_cndmask_b32_e64 v79, 0, 1, s[78:79]
	s_cmp_eq_u64 s[8:9], 0
	v_readfirstlane_b32 s8, v79
	s_cselect_b32 s8, s8, 2
	s_cmp_eq_u64 s[10:11], 0
	s_cselect_b32 s8, s8, 3
	s_cmp_eq_u64 s[12:13], 0
	s_cselect_b32 s8, s8, 4
	s_cmp_eq_u64 s[14:15], 0
	s_cselect_b32 s8, s8, 5
	s_cmp_eq_u64 s[16:17], 0
	s_cselect_b32 s8, s8, 6
	s_cmp_eq_u64 s[18:19], 0
	s_cselect_b32 s8, s8, 7
	s_cmp_eq_u64 s[20:21], 0
	s_cselect_b32 s8, s8, 8
	s_cmp_eq_u64 s[22:23], 0
	s_cselect_b32 s8, s8, 9
	s_cmp_eq_u64 s[24:25], 0
	s_cselect_b32 s8, s8, 10
	s_cmp_eq_u64 s[26:27], 0
	s_cselect_b32 s8, s8, 11
	s_cmp_eq_u64 s[28:29], 0
	s_cselect_b32 s8, s8, 12
	s_cmp_eq_u64 s[30:31], 0
	s_cselect_b32 s8, s8, 13
	s_cmp_eq_u64 s[34:35], 0
	s_cselect_b32 s8, s8, 14
	s_cmp_eq_u64 s[36:37], 0
	s_cselect_b32 s8, s8, 15
	s_cmp_eq_u64 s[38:39], 0
	s_cselect_b32 s8, s8, 16
	s_cmp_eq_u64 s[40:41], 0
	s_cselect_b32 s8, s8, 17
	s_cmp_eq_u64 s[42:43], 0
	v_cndmask_b32_e64 v79, 0, 1, s[0:1]
	s_cselect_b32 s8, s8, 18
	s_cmp_eq_u64 s[46:47], 0
	v_cmp_ne_u32_e32 vcc, 0, v79
	s_cselect_b32 s8, s8, 19
	s_cmp_eq_u64 vcc, 0
	s_cselect_b32 s8, s8, 20
	s_waitcnt lgkmcnt(0)
	v_max_u32_e32 v90, v90, v11
	v_max_u32_e32 v88, v88, v11
	v_max_u32_e32 v89, v89, v11
	v_max_u32_e32 v86, v86, v11
	v_max_u32_e32 v87, v87, v11
	v_max_u32_e32 v84, v84, v11
	v_max_u32_e32 v85, v85, v11
	v_max_u32_e32 v82, v82, v11
	v_max_u32_e32 v83, v83, v11
	v_max_u32_e32 v80, v80, v11
	v_max_u32_e32 v81, v81, v11
	v_max_u32_e32 v9, v9, v11
	v_max_u32_e32 v78, v78, v11
	v_max_u32_e32 v7, v7, v11
	v_max_u32_e32 v8, v8, v11
	v_max_u32_e32 v5, v5, v11
	v_max_u32_e32 v6, v6, v11
	v_max_u32_e32 v3, v3, v11
	v_max_u32_e32 v4, v4, v11
	v_max_u32_e32 v2, v2, v11
	v_sub_u32_e32 v90, v90, v11
	v_sub_u32_e32 v88, v88, v11
	v_sub_u32_e32 v89, v89, v11
	v_sub_u32_e32 v86, v86, v11
	v_sub_u32_e32 v87, v87, v11
	v_sub_u32_e32 v84, v84, v11
	v_sub_u32_e32 v85, v85, v11
	v_sub_u32_e32 v82, v82, v11
	v_sub_u32_e32 v83, v83, v11
	v_sub_u32_e32 v80, v80, v11
	v_sub_u32_e32 v81, v81, v11
	v_sub_u32_e32 v9, v9, v11
	v_sub_u32_e32 v78, v78, v11
	v_sub_u32_e32 v7, v7, v11
	v_sub_u32_e32 v8, v8, v11
	v_sub_u32_e32 v5, v5, v11
	v_sub_u32_e32 v6, v6, v11
	v_sub_u32_e32 v3, v3, v11
	v_sub_u32_e32 v4, v4, v11
	v_sub_u32_e32 v2, v2, v11
	s_lshl_b32 s10, s94, 23
	s_cmp_gt_u32 s8, 12
	s_mov_b64 s[0:1], -1
	s_cbranch_scc0 .LBB0_873
	s_cmp_lt_u32 s8, 17
	s_cbranch_scc1 .LBB0_826
	s_mov_b32 s0, 23
	s_mov_b32 s9, s10
